# C2 epilogue too: v_permlane16_swap pairing, 4 dwordx4 stores instead of 8 dwordx2 per unit and wave
# baseline (speedup 1.0000x reference)
; #define LAS __attribute__((address_space(3)))
; template <bool EMU> __device__ __forceinline__ float e2m3q(float y) { if constexpr (EMU) { y = fminf(fmaxf(y, -7.5f), 7.5f); return fabsf(y) < 1.f ? rintf(y * 8.f) * 0.125f : y; } else return y; }
;     static __device__ __forceinline__ f32x2 act2(f32x2 g, f32x2 l) {
;         g = __builtin_elementwise_min(g, (f32x2){7.f, 7.f}); l = __builtin_elementwise_min(__builtin_elementwise_max(l, (f32x2){-7.f, -7.f}), (f32x2){7.f, 7.f});
;         const f32x2 t = g * (-1.702f * 1.44269504089f); f32x2 e; e.x = __builtin_amdgcn_exp2f(t.x); e.y = __builtin_amdgcn_exp2f(t.y);
;         const f32x2 d = e + 1.0f; f32x2 r; r.x = __builtin_amdgcn_rcpf(d.x); r.y = __builtin_amdgcn_rcpf(d.y);
;         return (g * r) * (l * QS_ACT + QS_ACT);
;     __device__ __forceinline__ void operator()(const f32x4 (&acc)[2][2][4][2], const UnitD& u, int wr, int wc, int fr, int fq) const {
;         const int row0 = u.r0 + wr * 64 + fr, col0 = u.c0 + wc * 32 + 8 * fq;
;         const LAS float* bg = bl_lds + u.ui * 256 + wc * 32 + 8 * fq; const LAS float* bl = bg + 128;
;         f32x4 bgv[2], blv[2];
; #pragma unroll
;         for (int n = 0; n < 2; ++n) { bgv[n] = *(const LAS f32x4*)(bg + 4 * n); blv[n] = *(const LAS f32x4*)(bl + 4 * n); }
;         constexpr float SC = 1.f / (QS_X1 * QS_WUP);
; #pragma unroll
;         for (int ai = 0; ai < 2; ++ai)
; #pragma unroll
;             for (int m = 0; m < 4; ++m) { unsigned char* rowp = H + (size_t)(row0 + ai * 128 + m * 16) * DM + col0; u32x2 w;
; #pragma unroll
;                 for (int n = 0; n < 2; ++n) { const f32x4 g = acc[ai][0][m][n] * SC + bgv[n], l = acc[ai][1][m][n] * SC + blv[n];
;                     const f32x2 o0 = act2((f32x2){g[0], g[1]}, (f32x2){l[0], l[1]}), o1 = act2((f32x2){g[2], g[3]}, (f32x2){l[2], l[3]});
;                     int r = 0; r = __builtin_amdgcn_cvt_pk_fp8_f32(e2m3q<EMU_DOWN != 0>(o0.x), e2m3q<EMU_DOWN != 0>(o0.y), r, false); r = __builtin_amdgcn_cvt_pk_fp8_f32(e2m3q<EMU_DOWN != 0>(o1.x), e2m3q<EMU_DOWN != 0>(o1.y), r, true);
;                     if (n == 0) w.x = (unsigned)r; else w.y = (unsigned)r; }
;                 *(u32x2*)rowp = w; }
.LBB0_755:
	s_add_u32 s18, s85, 0xffffff00
	v_mov_b32_e32 v16, v154
	v_bfe_u32 v152, v154, 4, 1
	s_addc_u32 s19, s86, -1
	s_lshl_b32 s20, s76, 10
	v_mul_u32_u24_e32 v152, 0x3ff8, v152
	v_lshrrev_b32_e32 v0, 1, v16
	v_and_b32_e32 v18, 0x60, v0
	v_and_b32_e32 v19, 24, v0
	s_add_i32 s20, s20, 0
	s_add_i32 s20, s20, 0x23100
	v_lshlrev_b32_e32 v0, 2, v18
	v_lshlrev_b32_e32 v1, 2, v19
	v_add3_u32 v4, s20, v0, v1
	ds_read_b128 v[8:11], v4
	ds_read_b128 v[0:3], v4 offset:16
	ds_read_b128 v[12:15], v4 offset:512
	ds_read_b128 v[4:7], v4 offset:528
	v_and_b32_e32 v17, 15, v16
	s_waitcnt lgkmcnt(0)
	v_pk_fma_f32 v[22:23], v[148:149], s[36:37], v[8:9] op_sel_hi:[1,0,1]
	v_ashrrev_i32_e32 v20, 2, v16
	v_min_f32_e32 v23, 0x40e00000, v23
	v_min_f32_e32 v22, 0x40e00000, v22
	v_pk_mul_f32 v[176:177], v[22:23], s[78:79] op_sel_hi:[1,0]
	v_pk_fma_f32 v[174:175], v[116:117], s[36:37], v[12:13] op_sel_hi:[1,0,1]
	v_exp_f32_e32 v176, v176
	v_exp_f32_e32 v177, v177
	v_and_or_b32 v17, v20, s39, v17
	v_pk_fma_f32 v[20:21], v[150:151], s[36:37], v[10:11] op_sel_hi:[1,0,1]
	v_med3_f32 v175, v175, s47, v190
	v_pk_add_f32 v[176:177], v[176:177], 1.0 op_sel_hi:[1,0]
	v_med3_f32 v174, v174, s47, v190
	v_rcp_f32_e32 v176, v176
	v_rcp_f32_e32 v177, v177
	v_pk_fma_f32 v[174:175], v[174:175], 4.0, 4.0 op_sel_hi:[1,0,0]
	v_min_f32_e32 v21, 0x40e00000, v21
	v_min_f32_e32 v20, 0x40e00000, v20
	v_pk_mul_f32 v[22:23], v[22:23], v[176:177]
	v_pk_fma_f32 v[172:173], v[118:119], s[36:37], v[14:15] op_sel_hi:[1,0,1]
	v_pk_mul_f32 v[22:23], v[174:175], v[22:23]
	v_pk_mul_f32 v[174:175], v[20:21], s[78:79] op_sel_hi:[1,0]
	v_med3_f32 v173, v173, s47, v190
	v_exp_f32_e32 v174, v174
	v_exp_f32_e32 v175, v175
	v_med3_f32 v172, v172, s47, v190
	v_pk_fma_f32 v[172:173], v[172:173], 4.0, 4.0 op_sel_hi:[1,0,0]
	v_pk_fma_f32 v[176:177], v[112:113], s[36:37], v[4:5] op_sel_hi:[1,0,1]
	v_pk_add_f32 v[174:175], v[174:175], 1.0 op_sel_hi:[1,0]
	v_med3_f32 v177, v177, s47, v190
	v_rcp_f32_e32 v174, v174
	v_rcp_f32_e32 v175, v175
	v_med3_f32 v176, v176, s47, v190
	v_pk_fma_f32 v[176:177], v[176:177], 4.0, 4.0 op_sel_hi:[1,0,0]
	v_add3_u32 v16, v18, s2, v19
	v_pk_mul_f32 v[20:21], v[20:21], v[174:175]
	v_pk_fma_f32 v[174:175], v[114:115], s[36:37], v[6:7] op_sel_hi:[1,0,1]
	v_pk_mul_f32 v[20:21], v[172:173], v[20:21]
	v_mov_b32_e32 v172, v153
	v_cvt_pk_fp8_f32 v172, v22, v23
	v_pk_fma_f32 v[22:23], v[144:145], s[36:37], v[0:1] op_sel_hi:[1,0,1]
	v_mov_b32_e32 v173, v153
	v_min_f32_e32 v23, 0x40e00000, v23
	v_min_f32_e32 v22, 0x40e00000, v22
	v_pk_mul_f32 v[178:179], v[22:23], s[78:79] op_sel_hi:[1,0]
	v_cvt_pk_fp8_f32 v172, v20, v21 op_sel:[0,0,1]
	v_exp_f32_e32 v178, v178
	v_exp_f32_e32 v179, v179
	v_pk_fma_f32 v[20:21], v[146:147], s[36:37], v[2:3] op_sel_hi:[1,0,1]
	v_med3_f32 v175, v175, s47, v190
	v_min_f32_e32 v21, 0x40e00000, v21
	v_pk_add_f32 v[178:179], v[178:179], 1.0 op_sel_hi:[1,0]
	v_min_f32_e32 v20, 0x40e00000, v20
	v_rcp_f32_e32 v178, v178
	v_rcp_f32_e32 v179, v179
	v_med3_f32 v174, v174, s47, v190
	v_pk_fma_f32 v[174:175], v[174:175], 4.0, 4.0 op_sel_hi:[1,0,0]
	v_add_u32_e32 v18, s68, v17
	v_pk_mul_f32 v[22:23], v[22:23], v[178:179]
	v_ashrrev_i32_e32 v19, 31, v18
	v_pk_mul_f32 v[22:23], v[176:177], v[22:23]
	v_pk_mul_f32 v[176:177], v[20:21], s[78:79] op_sel_hi:[1,0]
	v_cvt_pk_fp8_f32 v173, v22, v23
	v_exp_f32_e32 v176, v176
	v_exp_f32_e32 v177, v177
	v_lshlrev_b64 v[18:19], 10, v[18:19]
	v_ashrrev_i32_e32 v17, 31, v16
	v_lshl_add_u64 v[18:19], s[6:7], 0, v[18:19]
	v_pk_add_f32 v[176:177], v[176:177], 1.0 op_sel_hi:[1,0]
	v_lshl_add_u64 v[16:17], v[18:19], 0, v[16:17]
	s_nop 0
	v_lshl_add_u64 v[144:145], v[16:17], 0, v[152:153]
	v_rcp_f32_e32 v176, v176
	v_rcp_f32_e32 v177, v177
	v_pk_fma_f32 v[18:19], v[142:143], s[36:37], v[10:11] op_sel_hi:[1,0,1]
	v_pk_fma_f32 v[22:23], v[110:111], s[36:37], v[14:15] op_sel_hi:[1,0,1]
	v_min_f32_e32 v19, 0x40e00000, v19
	v_pk_mul_f32 v[20:21], v[20:21], v[176:177]
	v_min_f32_e32 v18, 0x40e00000, v18
	v_pk_mul_f32 v[20:21], v[174:175], v[20:21]
	v_med3_f32 v23, v23, s47, v190
	v_cvt_pk_fp8_f32 v173, v20, v21 op_sel:[0,0,1]
	v_pk_fma_f32 v[20:21], v[140:141], s[36:37], v[8:9] op_sel_hi:[1,0,1]
	v_med3_f32 v22, v22, s47, v190
	v_min_f32_e32 v21, 0x40e00000, v21
	v_min_f32_e32 v20, 0x40e00000, v20
	v_pk_mul_f32 v[174:175], v[20:21], s[78:79] op_sel_hi:[1,0]
	v_mov_b32_e32 v148, v172
	v_mov_b32_e32 v149, v173
	v_exp_f32_e32 v174, v174
	v_exp_f32_e32 v175, v175
	v_pk_fma_f32 v[172:173], v[108:109], s[36:37], v[12:13] op_sel_hi:[1,0,1]
	v_pk_fma_f32 v[22:23], v[22:23], 4.0, 4.0 op_sel_hi:[1,0,0]
	v_med3_f32 v173, v173, s47, v190
	v_pk_add_f32 v[174:175], v[174:175], 1.0 op_sel_hi:[1,0]
	v_med3_f32 v172, v172, s47, v190
	v_rcp_f32_e32 v174, v174
	v_rcp_f32_e32 v175, v175
	v_pk_fma_f32 v[172:173], v[172:173], 4.0, 4.0 op_sel_hi:[1,0,0]
	s_movk_i32 s20, 0x4000
	s_mov_b64 s[88:89], 0x42040080
	v_pk_mul_f32 v[20:21], v[20:21], v[174:175]
	v_pk_fma_f32 v[174:175], v[104:105], s[36:37], v[4:5] op_sel_hi:[1,0,1]
	v_pk_mul_f32 v[20:21], v[172:173], v[20:21]
	v_pk_mul_f32 v[172:173], v[18:19], s[78:79] op_sel_hi:[1,0]
	v_med3_f32 v175, v175, s47, v190
	v_exp_f32_e32 v172, v172
	v_exp_f32_e32 v173, v173
	v_med3_f32 v174, v174, s47, v190
	v_pk_fma_f32 v[174:175], v[174:175], 4.0, 4.0 op_sel_hi:[1,0,0]
	v_pk_add_f32 v[172:173], v[172:173], 1.0 op_sel_hi:[1,0]
	s_nop 0
	v_rcp_f32_e32 v172, v172
	v_rcp_f32_e32 v173, v173
	s_nop 0
	v_pk_mul_f32 v[18:19], v[18:19], v[172:173]
	s_nop 0
	v_pk_mul_f32 v[18:19], v[22:23], v[18:19]
	v_mov_b32_e32 v22, v153
	v_cvt_pk_fp8_f32 v22, v20, v21
	v_pk_fma_f32 v[20:21], v[136:137], s[36:37], v[0:1] op_sel_hi:[1,0,1]
; #define LAS __attribute__((address_space(3)))
; template <bool EMU> __device__ __forceinline__ float e2m3q(float y) { if constexpr (EMU) { y = fminf(fmaxf(y, -7.5f), 7.5f); return fabsf(y) < 1.f ? rintf(y * 8.f) * 0.125f : y; } else return y; }
;     static __device__ __forceinline__ f32x2 act2(f32x2 g, f32x2 l) {
;         g = __builtin_elementwise_min(g, (f32x2){7.f, 7.f}); l = __builtin_elementwise_min(__builtin_elementwise_max(l, (f32x2){-7.f, -7.f}), (f32x2){7.f, 7.f});
;         const f32x2 t = g * (-1.702f * 1.44269504089f); f32x2 e; e.x = __builtin_amdgcn_exp2f(t.x); e.y = __builtin_amdgcn_exp2f(t.y);
;         const f32x2 d = e + 1.0f; f32x2 r; r.x = __builtin_amdgcn_rcpf(d.x); r.y = __builtin_amdgcn_rcpf(d.y);
;         return (g * r) * (l * QS_ACT + QS_ACT);
;     __device__ __forceinline__ void operator()(const f32x4 (&acc)[2][2][4][2], const UnitD& u, int wr, int wc, int fr, int fq) const {
;         const int row0 = u.r0 + wr * 64 + fr, col0 = u.c0 + wc * 32 + 8 * fq;
;         const LAS float* bg = bl_lds + u.ui * 256 + wc * 32 + 8 * fq; const LAS float* bl = bg + 128;
;         f32x4 bgv[2], blv[2];
; #pragma unroll
;         for (int n = 0; n < 2; ++n) { bgv[n] = *(const LAS f32x4*)(bg + 4 * n); blv[n] = *(const LAS f32x4*)(bl + 4 * n); }
;         constexpr float SC = 1.f / (QS_X1 * QS_WUP);
; #pragma unroll
;         for (int ai = 0; ai < 2; ++ai)
; #pragma unroll
;             for (int m = 0; m < 4; ++m) { unsigned char* rowp = H + (size_t)(row0 + ai * 128 + m * 16) * DM + col0; u32x2 w;
; #pragma unroll
;                 for (int n = 0; n < 2; ++n) { const f32x4 g = acc[ai][0][m][n] * SC + bgv[n], l = acc[ai][1][m][n] * SC + blv[n];
;                     const f32x2 o0 = act2((f32x2){g[0], g[1]}, (f32x2){l[0], l[1]}), o1 = act2((f32x2){g[2], g[3]}, (f32x2){l[2], l[3]});
;                     int r = 0; r = __builtin_amdgcn_cvt_pk_fp8_f32(e2m3q<EMU_DOWN != 0>(o0.x), e2m3q<EMU_DOWN != 0>(o0.y), r, false); r = __builtin_amdgcn_cvt_pk_fp8_f32(e2m3q<EMU_DOWN != 0>(o1.x), e2m3q<EMU_DOWN != 0>(o1.y), r, true);
;                     if (n == 0) w.x = (unsigned)r; else w.y = (unsigned)r; }
;                 *(u32x2*)rowp = w; }
	v_mov_b32_e32 v23, v153
	v_min_f32_e32 v21, 0x40e00000, v21
	v_min_f32_e32 v20, 0x40e00000, v20
	v_pk_mul_f32 v[176:177], v[20:21], s[78:79] op_sel_hi:[1,0]
	v_cvt_pk_fp8_f32 v22, v18, v19 op_sel:[0,0,1]
	v_exp_f32_e32 v176, v176
	v_exp_f32_e32 v177, v177
	v_pk_fma_f32 v[18:19], v[138:139], s[36:37], v[2:3] op_sel_hi:[1,0,1]
	v_pk_fma_f32 v[172:173], v[106:107], s[36:37], v[6:7] op_sel_hi:[1,0,1]
	v_min_f32_e32 v19, 0x40e00000, v19
	v_pk_add_f32 v[176:177], v[176:177], 1.0 op_sel_hi:[1,0]
	v_min_f32_e32 v18, 0x40e00000, v18
	v_rcp_f32_e32 v176, v176
	v_rcp_f32_e32 v177, v177
	v_med3_f32 v173, v173, s47, v190
	v_med3_f32 v172, v172, s47, v190
	v_pk_fma_f32 v[172:173], v[172:173], 4.0, 4.0 op_sel_hi:[1,0,0]
	v_pk_mul_f32 v[20:21], v[20:21], v[176:177]
	s_nop 0
	v_pk_mul_f32 v[20:21], v[174:175], v[20:21]
	v_pk_mul_f32 v[174:175], v[18:19], s[78:79] op_sel_hi:[1,0]
	v_cvt_pk_fp8_f32 v23, v20, v21
	v_exp_f32_e32 v174, v174
	v_exp_f32_e32 v175, v175
	v_pk_fma_f32 v[20:21], v[132:133], s[36:37], v[8:9] op_sel_hi:[1,0,1]
	v_pk_add_f32 v[174:175], v[174:175], 1.0 op_sel_hi:[1,0]
	s_nop 0
	v_rcp_f32_e32 v174, v174
	v_rcp_f32_e32 v175, v175
	v_min_f32_e32 v21, 0x40e00000, v21
	v_min_f32_e32 v20, 0x40e00000, v20
	v_pk_mul_f32 v[18:19], v[18:19], v[174:175]
	v_pk_mul_f32 v[174:175], v[20:21], s[78:79] op_sel_hi:[1,0]
	v_pk_mul_f32 v[18:19], v[172:173], v[18:19]
	v_exp_f32_e32 v174, v174
	v_exp_f32_e32 v175, v175
	v_cvt_pk_fp8_f32 v23, v18, v19 op_sel:[0,0,1]
	v_add_co_u32_e32 v18, vcc, s20, v16
	v_pk_add_f32 v[174:175], v[174:175], 1.0 op_sel_hi:[1,0]
	s_nop 0
	v_addc_co_u32_e32 v19, vcc, 0, v17, vcc
	v_rcp_f32_e32 v174, v174
	v_rcp_f32_e32 v175, v175
	v_pk_fma_f32 v[172:173], v[100:101], s[36:37], v[12:13] op_sel_hi:[1,0,1]
	v_mov_b32_e32 v150, v22
	v_mov_b32_e32 v151, v23
	s_nop 1
	v_permlane16_swap_b32_e32 v148, v150
	v_permlane16_swap_b32_e32 v149, v151
	global_store_dwordx4 v[144:145], v[148:151], off
	v_pk_fma_f32 v[18:19], v[134:135], s[36:37], v[10:11] op_sel_hi:[1,0,1]
	v_med3_f32 v173, v173, s47, v190
	v_med3_f32 v172, v172, s47, v190
	v_pk_mul_f32 v[20:21], v[20:21], v[174:175]
	v_pk_fma_f32 v[172:173], v[172:173], 4.0, 4.0 op_sel_hi:[1,0,0]
	v_min_f32_e32 v19, 0x40e00000, v19
	v_min_f32_e32 v18, 0x40e00000, v18
	v_pk_mul_f32 v[20:21], v[172:173], v[20:21]
	v_pk_mul_f32 v[172:173], v[18:19], s[78:79] op_sel_hi:[1,0]
	v_pk_fma_f32 v[22:23], v[102:103], s[36:37], v[14:15] op_sel_hi:[1,0,1]
	v_exp_f32_e32 v172, v172
	v_exp_f32_e32 v173, v173
	v_med3_f32 v23, v23, s47, v190
	v_med3_f32 v22, v22, s47, v190
	v_pk_fma_f32 v[22:23], v[22:23], 4.0, 4.0 op_sel_hi:[1,0,0]
	v_pk_add_f32 v[172:173], v[172:173], 1.0 op_sel_hi:[1,0]
	v_pk_fma_f32 v[174:175], v[96:97], s[36:37], v[4:5] op_sel_hi:[1,0,1]
	v_rcp_f32_e32 v172, v172
	v_rcp_f32_e32 v173, v173
	v_med3_f32 v175, v175, s47, v190
	v_med3_f32 v174, v174, s47, v190
	v_pk_fma_f32 v[174:175], v[174:175], 4.0, 4.0 op_sel_hi:[1,0,0]
	v_pk_mul_f32 v[18:19], v[18:19], v[172:173]
	v_pk_fma_f32 v[172:173], v[98:99], s[36:37], v[6:7] op_sel_hi:[1,0,1]
	v_pk_mul_f32 v[18:19], v[22:23], v[18:19]
	v_mov_b32_e32 v22, v153
	v_cvt_pk_fp8_f32 v22, v20, v21
	v_pk_fma_f32 v[20:21], v[128:129], s[36:37], v[0:1] op_sel_hi:[1,0,1]
	v_mov_b32_e32 v23, v153
	v_min_f32_e32 v21, 0x40e00000, v21
	v_min_f32_e32 v20, 0x40e00000, v20
	v_pk_mul_f32 v[176:177], v[20:21], s[78:79] op_sel_hi:[1,0]
	v_cvt_pk_fp8_f32 v22, v18, v19 op_sel:[0,0,1]
	v_exp_f32_e32 v176, v176
	v_exp_f32_e32 v177, v177
	v_pk_fma_f32 v[18:19], v[130:131], s[36:37], v[2:3] op_sel_hi:[1,0,1]
	v_med3_f32 v173, v173, s47, v190
	v_min_f32_e32 v19, 0x40e00000, v19
	v_pk_add_f32 v[176:177], v[176:177], 1.0 op_sel_hi:[1,0]
	v_min_f32_e32 v18, 0x40e00000, v18
	v_rcp_f32_e32 v176, v176
	v_rcp_f32_e32 v177, v177
	v_med3_f32 v172, v172, s47, v190
	v_pk_fma_f32 v[172:173], v[172:173], 4.0, 4.0 op_sel_hi:[1,0,0]
	s_mov_b32 s20, 0x8000
	v_pk_mul_f32 v[20:21], v[20:21], v[176:177]
	s_nop 0
	v_pk_mul_f32 v[20:21], v[174:175], v[20:21]
	v_pk_mul_f32 v[174:175], v[18:19], s[78:79] op_sel_hi:[1,0]
	v_cvt_pk_fp8_f32 v23, v20, v21
	v_exp_f32_e32 v174, v174
	v_exp_f32_e32 v175, v175
	v_pk_fma_f32 v[20:21], v[124:125], s[36:37], v[8:9] op_sel_hi:[1,0,1]
	v_pk_add_f32 v[174:175], v[174:175], 1.0 op_sel_hi:[1,0]
	s_nop 0
	v_rcp_f32_e32 v174, v174
	v_rcp_f32_e32 v175, v175
	v_min_f32_e32 v21, 0x40e00000, v21
	v_min_f32_e32 v20, 0x40e00000, v20
	v_pk_mul_f32 v[18:19], v[18:19], v[174:175]
	v_pk_mul_f32 v[174:175], v[20:21], s[78:79] op_sel_hi:[1,0]
	v_pk_mul_f32 v[18:19], v[172:173], v[18:19]
	v_exp_f32_e32 v174, v174
	v_exp_f32_e32 v175, v175
	v_cvt_pk_fp8_f32 v23, v18, v19 op_sel:[0,0,1]
	v_add_co_u32_e32 v18, vcc, s20, v16
	v_pk_add_f32 v[174:175], v[174:175], 1.0 op_sel_hi:[1,0]
	s_nop 0
	v_addc_co_u32_e32 v19, vcc, 0, v17, vcc
	v_rcp_f32_e32 v174, v174
	v_rcp_f32_e32 v175, v175
	v_pk_fma_f32 v[172:173], v[92:93], s[36:37], v[12:13] op_sel_hi:[1,0,1]
	v_mov_b32_e32 v148, v22
	v_mov_b32_e32 v149, v23
	v_lshl_add_u64 v[146:147], v[18:19], 0, v[152:153]
	v_pk_fma_f32 v[18:19], v[126:127], s[36:37], v[10:11] op_sel_hi:[1,0,1]
	v_med3_f32 v173, v173, s47, v190
	v_med3_f32 v172, v172, s47, v190
	v_pk_mul_f32 v[20:21], v[20:21], v[174:175]
	v_pk_fma_f32 v[172:173], v[172:173], 4.0, 4.0 op_sel_hi:[1,0,0]
	v_min_f32_e32 v19, 0x40e00000, v19
	v_min_f32_e32 v18, 0x40e00000, v18
	v_pk_mul_f32 v[20:21], v[172:173], v[20:21]
	v_pk_mul_f32 v[172:173], v[18:19], s[78:79] op_sel_hi:[1,0]
	v_pk_fma_f32 v[22:23], v[94:95], s[36:37], v[14:15] op_sel_hi:[1,0,1]
	v_exp_f32_e32 v172, v172
	v_exp_f32_e32 v173, v173
	v_med3_f32 v23, v23, s47, v190
	v_med3_f32 v22, v22, s47, v190
; #define LAS __attribute__((address_space(3)))
; template <bool EMU> __device__ __forceinline__ float e2m3q(float y) { if constexpr (EMU) { y = fminf(fmaxf(y, -7.5f), 7.5f); return fabsf(y) < 1.f ? rintf(y * 8.f) * 0.125f : y; } else return y; }
;     static __device__ __forceinline__ f32x2 act2(f32x2 g, f32x2 l) {
;         g = __builtin_elementwise_min(g, (f32x2){7.f, 7.f}); l = __builtin_elementwise_min(__builtin_elementwise_max(l, (f32x2){-7.f, -7.f}), (f32x2){7.f, 7.f});
;         const f32x2 t = g * (-1.702f * 1.44269504089f); f32x2 e; e.x = __builtin_amdgcn_exp2f(t.x); e.y = __builtin_amdgcn_exp2f(t.y);
;         const f32x2 d = e + 1.0f; f32x2 r; r.x = __builtin_amdgcn_rcpf(d.x); r.y = __builtin_amdgcn_rcpf(d.y);
;         return (g * r) * (l * QS_ACT + QS_ACT);
;     __device__ __forceinline__ void operator()(const f32x4 (&acc)[2][2][4][2], const UnitD& u, int wr, int wc, int fr, int fq) const {
;         const int row0 = u.r0 + wr * 64 + fr, col0 = u.c0 + wc * 32 + 8 * fq;
;         const LAS float* bg = bl_lds + u.ui * 256 + wc * 32 + 8 * fq; const LAS float* bl = bg + 128;
;         f32x4 bgv[2], blv[2];
; #pragma unroll
;         for (int n = 0; n < 2; ++n) { bgv[n] = *(const LAS f32x4*)(bg + 4 * n); blv[n] = *(const LAS f32x4*)(bl + 4 * n); }
;         constexpr float SC = 1.f / (QS_X1 * QS_WUP);
; #pragma unroll
;         for (int ai = 0; ai < 2; ++ai)
; #pragma unroll
;             for (int m = 0; m < 4; ++m) { unsigned char* rowp = H + (size_t)(row0 + ai * 128 + m * 16) * DM + col0; u32x2 w;
; #pragma unroll
;                 for (int n = 0; n < 2; ++n) { const f32x4 g = acc[ai][0][m][n] * SC + bgv[n], l = acc[ai][1][m][n] * SC + blv[n];
;                     const f32x2 o0 = act2((f32x2){g[0], g[1]}, (f32x2){l[0], l[1]}), o1 = act2((f32x2){g[2], g[3]}, (f32x2){l[2], l[3]});
;                     int r = 0; r = __builtin_amdgcn_cvt_pk_fp8_f32(e2m3q<EMU_DOWN != 0>(o0.x), e2m3q<EMU_DOWN != 0>(o0.y), r, false); r = __builtin_amdgcn_cvt_pk_fp8_f32(e2m3q<EMU_DOWN != 0>(o1.x), e2m3q<EMU_DOWN != 0>(o1.y), r, true);
;                     if (n == 0) w.x = (unsigned)r; else w.y = (unsigned)r; }
;                 *(u32x2*)rowp = w; }
	v_pk_fma_f32 v[22:23], v[22:23], 4.0, 4.0 op_sel_hi:[1,0,0]
	v_pk_add_f32 v[172:173], v[172:173], 1.0 op_sel_hi:[1,0]
	v_pk_fma_f32 v[174:175], v[88:89], s[36:37], v[4:5] op_sel_hi:[1,0,1]
	v_rcp_f32_e32 v172, v172
	v_rcp_f32_e32 v173, v173
	v_med3_f32 v175, v175, s47, v190
	v_med3_f32 v174, v174, s47, v190
	v_pk_fma_f32 v[174:175], v[174:175], 4.0, 4.0 op_sel_hi:[1,0,0]
	v_pk_mul_f32 v[18:19], v[18:19], v[172:173]
	v_pk_fma_f32 v[172:173], v[90:91], s[36:37], v[6:7] op_sel_hi:[1,0,1]
	v_pk_mul_f32 v[18:19], v[22:23], v[18:19]
	v_mov_b32_e32 v22, v153
	v_cvt_pk_fp8_f32 v22, v20, v21
	v_pk_fma_f32 v[20:21], v[120:121], s[36:37], v[0:1] op_sel_hi:[1,0,1]
	v_mov_b32_e32 v23, v153
	v_min_f32_e32 v21, 0x40e00000, v21
	v_min_f32_e32 v20, 0x40e00000, v20
	v_pk_mul_f32 v[176:177], v[20:21], s[78:79] op_sel_hi:[1,0]
	v_cvt_pk_fp8_f32 v22, v18, v19 op_sel:[0,0,1]
	v_exp_f32_e32 v176, v176
	v_exp_f32_e32 v177, v177
	v_pk_fma_f32 v[18:19], v[122:123], s[36:37], v[2:3] op_sel_hi:[1,0,1]
	v_med3_f32 v173, v173, s47, v190
	v_min_f32_e32 v19, 0x40e00000, v19
	v_pk_add_f32 v[176:177], v[176:177], 1.0 op_sel_hi:[1,0]
	v_min_f32_e32 v18, 0x40e00000, v18
	v_rcp_f32_e32 v176, v176
	v_rcp_f32_e32 v177, v177
	v_med3_f32 v172, v172, s47, v190
	v_pk_fma_f32 v[172:173], v[172:173], 4.0, 4.0 op_sel_hi:[1,0,0]
	s_mov_b32 s20, 0xc000
	v_pk_mul_f32 v[20:21], v[20:21], v[176:177]
	s_nop 0
	v_pk_mul_f32 v[20:21], v[174:175], v[20:21]
	v_pk_mul_f32 v[174:175], v[18:19], s[78:79] op_sel_hi:[1,0]
	v_cvt_pk_fp8_f32 v23, v20, v21
	v_exp_f32_e32 v174, v174
	v_exp_f32_e32 v175, v175
	v_pk_fma_f32 v[20:21], v[84:85], s[36:37], v[8:9] op_sel_hi:[1,0,1]
	v_pk_add_f32 v[174:175], v[174:175], 1.0 op_sel_hi:[1,0]
	s_nop 0
	v_rcp_f32_e32 v174, v174
	v_rcp_f32_e32 v175, v175
	v_min_f32_e32 v21, 0x40e00000, v21
	v_min_f32_e32 v20, 0x40e00000, v20
	v_pk_mul_f32 v[18:19], v[18:19], v[174:175]
	v_pk_mul_f32 v[174:175], v[20:21], s[78:79] op_sel_hi:[1,0]
	v_pk_mul_f32 v[18:19], v[172:173], v[18:19]
	v_exp_f32_e32 v174, v174
	v_exp_f32_e32 v175, v175
	v_cvt_pk_fp8_f32 v23, v18, v19 op_sel:[0,0,1]
	v_add_co_u32_e32 v18, vcc, s20, v16
	v_pk_add_f32 v[174:175], v[174:175], 1.0 op_sel_hi:[1,0]
	s_nop 0
	v_addc_co_u32_e32 v19, vcc, 0, v17, vcc
	v_rcp_f32_e32 v174, v174
	v_rcp_f32_e32 v175, v175
	v_pk_fma_f32 v[172:173], v[52:53], s[36:37], v[12:13] op_sel_hi:[1,0,1]
	v_mov_b32_e32 v150, v22
	v_mov_b32_e32 v151, v23
	s_nop 1
	v_permlane16_swap_b32_e32 v148, v150
	v_permlane16_swap_b32_e32 v149, v151
	global_store_dwordx4 v[146:147], v[148:151], off
	v_pk_fma_f32 v[18:19], v[86:87], s[36:37], v[10:11] op_sel_hi:[1,0,1]
	v_med3_f32 v173, v173, s47, v190
	v_med3_f32 v172, v172, s47, v190
	v_pk_mul_f32 v[20:21], v[20:21], v[174:175]
	v_pk_fma_f32 v[172:173], v[172:173], 4.0, 4.0 op_sel_hi:[1,0,0]
	v_min_f32_e32 v19, 0x40e00000, v19
	v_min_f32_e32 v18, 0x40e00000, v18
	v_pk_mul_f32 v[20:21], v[172:173], v[20:21]
	v_pk_mul_f32 v[172:173], v[18:19], s[78:79] op_sel_hi:[1,0]
	v_pk_fma_f32 v[22:23], v[54:55], s[36:37], v[14:15] op_sel_hi:[1,0,1]
	v_exp_f32_e32 v172, v172
	v_exp_f32_e32 v173, v173
	v_med3_f32 v23, v23, s47, v190
	v_med3_f32 v22, v22, s47, v190
	v_pk_fma_f32 v[22:23], v[22:23], 4.0, 4.0 op_sel_hi:[1,0,0]
	v_pk_add_f32 v[172:173], v[172:173], 1.0 op_sel_hi:[1,0]
	v_pk_fma_f32 v[174:175], v[48:49], s[36:37], v[4:5] op_sel_hi:[1,0,1]
	v_rcp_f32_e32 v172, v172
	v_rcp_f32_e32 v173, v173
	v_med3_f32 v175, v175, s47, v190
	v_med3_f32 v174, v174, s47, v190
	v_pk_fma_f32 v[174:175], v[174:175], 4.0, 4.0 op_sel_hi:[1,0,0]
	v_pk_mul_f32 v[18:19], v[18:19], v[172:173]
	v_pk_fma_f32 v[172:173], v[50:51], s[36:37], v[6:7] op_sel_hi:[1,0,1]
	v_pk_mul_f32 v[18:19], v[22:23], v[18:19]
	v_mov_b32_e32 v22, v153
	v_cvt_pk_fp8_f32 v22, v20, v21
	v_pk_fma_f32 v[20:21], v[80:81], s[36:37], v[0:1] op_sel_hi:[1,0,1]
	v_mov_b32_e32 v23, v153
	v_min_f32_e32 v21, 0x40e00000, v21
	v_min_f32_e32 v20, 0x40e00000, v20
	v_pk_mul_f32 v[176:177], v[20:21], s[78:79] op_sel_hi:[1,0]
	v_cvt_pk_fp8_f32 v22, v18, v19 op_sel:[0,0,1]
	v_exp_f32_e32 v176, v176
	v_exp_f32_e32 v177, v177
	v_pk_fma_f32 v[18:19], v[82:83], s[36:37], v[2:3] op_sel_hi:[1,0,1]
	v_med3_f32 v173, v173, s47, v190
	v_min_f32_e32 v19, 0x40e00000, v19
	v_pk_add_f32 v[176:177], v[176:177], 1.0 op_sel_hi:[1,0]
	v_min_f32_e32 v18, 0x40e00000, v18
	v_rcp_f32_e32 v176, v176
	v_rcp_f32_e32 v177, v177
	v_med3_f32 v172, v172, s47, v190
	v_pk_fma_f32 v[172:173], v[172:173], 4.0, 4.0 op_sel_hi:[1,0,0]
	s_mov_b32 s20, 0x20000
	v_pk_mul_f32 v[20:21], v[20:21], v[176:177]
	s_nop 0
	v_pk_mul_f32 v[20:21], v[174:175], v[20:21]
	v_pk_mul_f32 v[174:175], v[18:19], s[78:79] op_sel_hi:[1,0]
	v_cvt_pk_fp8_f32 v23, v20, v21
	v_exp_f32_e32 v174, v174
	v_exp_f32_e32 v175, v175
	v_pk_fma_f32 v[20:21], v[76:77], s[36:37], v[8:9] op_sel_hi:[1,0,1]
	v_pk_add_f32 v[174:175], v[174:175], 1.0 op_sel_hi:[1,0]
	s_nop 0
	v_rcp_f32_e32 v174, v174
	v_rcp_f32_e32 v175, v175
	v_min_f32_e32 v21, 0x40e00000, v21
	v_min_f32_e32 v20, 0x40e00000, v20
	v_pk_mul_f32 v[18:19], v[18:19], v[174:175]
	v_pk_mul_f32 v[174:175], v[20:21], s[78:79] op_sel_hi:[1,0]
	v_pk_mul_f32 v[18:19], v[172:173], v[18:19]
	v_exp_f32_e32 v174, v174
	v_exp_f32_e32 v175, v175
	v_cvt_pk_fp8_f32 v23, v18, v19 op_sel:[0,0,1]
	v_add_co_u32_e32 v18, vcc, s20, v16
	v_pk_add_f32 v[174:175], v[174:175], 1.0 op_sel_hi:[1,0]
	s_nop 0
	v_addc_co_u32_e32 v19, vcc, 0, v17, vcc
	v_rcp_f32_e32 v174, v174
	v_rcp_f32_e32 v175, v175
	v_pk_fma_f32 v[172:173], v[44:45], s[36:37], v[12:13] op_sel_hi:[1,0,1]
	v_mov_b32_e32 v148, v22
	v_mov_b32_e32 v149, v23
	v_lshl_add_u64 v[146:147], v[18:19], 0, v[152:153]
	v_pk_fma_f32 v[18:19], v[78:79], s[36:37], v[10:11] op_sel_hi:[1,0,1]
; #define LAS __attribute__((address_space(3)))
; template <bool EMU> __device__ __forceinline__ float e2m3q(float y) { if constexpr (EMU) { y = fminf(fmaxf(y, -7.5f), 7.5f); return fabsf(y) < 1.f ? rintf(y * 8.f) * 0.125f : y; } else return y; }
;     static __device__ __forceinline__ f32x2 act2(f32x2 g, f32x2 l) {
;         g = __builtin_elementwise_min(g, (f32x2){7.f, 7.f}); l = __builtin_elementwise_min(__builtin_elementwise_max(l, (f32x2){-7.f, -7.f}), (f32x2){7.f, 7.f});
;         const f32x2 t = g * (-1.702f * 1.44269504089f); f32x2 e; e.x = __builtin_amdgcn_exp2f(t.x); e.y = __builtin_amdgcn_exp2f(t.y);
;         const f32x2 d = e + 1.0f; f32x2 r; r.x = __builtin_amdgcn_rcpf(d.x); r.y = __builtin_amdgcn_rcpf(d.y);
;         return (g * r) * (l * QS_ACT + QS_ACT);
;     __device__ __forceinline__ void operator()(const f32x4 (&acc)[2][2][4][2], const UnitD& u, int wr, int wc, int fr, int fq) const {
;         const int row0 = u.r0 + wr * 64 + fr, col0 = u.c0 + wc * 32 + 8 * fq;
;         const LAS float* bg = bl_lds + u.ui * 256 + wc * 32 + 8 * fq; const LAS float* bl = bg + 128;
;         f32x4 bgv[2], blv[2];
; #pragma unroll
;         for (int n = 0; n < 2; ++n) { bgv[n] = *(const LAS f32x4*)(bg + 4 * n); blv[n] = *(const LAS f32x4*)(bl + 4 * n); }
;         constexpr float SC = 1.f / (QS_X1 * QS_WUP);
; #pragma unroll
;         for (int ai = 0; ai < 2; ++ai)
; #pragma unroll
;             for (int m = 0; m < 4; ++m) { unsigned char* rowp = H + (size_t)(row0 + ai * 128 + m * 16) * DM + col0; u32x2 w;
; #pragma unroll
;                 for (int n = 0; n < 2; ++n) { const f32x4 g = acc[ai][0][m][n] * SC + bgv[n], l = acc[ai][1][m][n] * SC + blv[n];
;                     const f32x2 o0 = act2((f32x2){g[0], g[1]}, (f32x2){l[0], l[1]}), o1 = act2((f32x2){g[2], g[3]}, (f32x2){l[2], l[3]});
;                     int r = 0; r = __builtin_amdgcn_cvt_pk_fp8_f32(e2m3q<EMU_DOWN != 0>(o0.x), e2m3q<EMU_DOWN != 0>(o0.y), r, false); r = __builtin_amdgcn_cvt_pk_fp8_f32(e2m3q<EMU_DOWN != 0>(o1.x), e2m3q<EMU_DOWN != 0>(o1.y), r, true);
;                     if (n == 0) w.x = (unsigned)r; else w.y = (unsigned)r; }
;                 *(u32x2*)rowp = w; }
	v_med3_f32 v173, v173, s47, v190
	v_med3_f32 v172, v172, s47, v190
	v_pk_mul_f32 v[20:21], v[20:21], v[174:175]
	v_pk_fma_f32 v[172:173], v[172:173], 4.0, 4.0 op_sel_hi:[1,0,0]
	v_min_f32_e32 v19, 0x40e00000, v19
	v_min_f32_e32 v18, 0x40e00000, v18
	v_pk_mul_f32 v[20:21], v[172:173], v[20:21]
	v_pk_mul_f32 v[172:173], v[18:19], s[78:79] op_sel_hi:[1,0]
	v_pk_fma_f32 v[22:23], v[46:47], s[36:37], v[14:15] op_sel_hi:[1,0,1]
	v_exp_f32_e32 v172, v172
	v_exp_f32_e32 v173, v173
	v_med3_f32 v23, v23, s47, v190
	v_med3_f32 v22, v22, s47, v190
	v_pk_fma_f32 v[22:23], v[22:23], 4.0, 4.0 op_sel_hi:[1,0,0]
	v_pk_add_f32 v[172:173], v[172:173], 1.0 op_sel_hi:[1,0]
	v_pk_fma_f32 v[174:175], v[40:41], s[36:37], v[4:5] op_sel_hi:[1,0,1]
	v_rcp_f32_e32 v172, v172
	v_rcp_f32_e32 v173, v173
	v_med3_f32 v175, v175, s47, v190
	v_med3_f32 v174, v174, s47, v190
	v_pk_fma_f32 v[174:175], v[174:175], 4.0, 4.0 op_sel_hi:[1,0,0]
	v_pk_mul_f32 v[18:19], v[18:19], v[172:173]
	v_pk_fma_f32 v[172:173], v[42:43], s[36:37], v[6:7] op_sel_hi:[1,0,1]
	v_pk_mul_f32 v[18:19], v[22:23], v[18:19]
	v_mov_b32_e32 v22, v153
	v_cvt_pk_fp8_f32 v22, v20, v21
	v_pk_fma_f32 v[20:21], v[72:73], s[36:37], v[0:1] op_sel_hi:[1,0,1]
	v_mov_b32_e32 v23, v153
	v_min_f32_e32 v21, 0x40e00000, v21
	v_min_f32_e32 v20, 0x40e00000, v20
	v_pk_mul_f32 v[176:177], v[20:21], s[78:79] op_sel_hi:[1,0]
	v_cvt_pk_fp8_f32 v22, v18, v19 op_sel:[0,0,1]
	v_exp_f32_e32 v176, v176
	v_exp_f32_e32 v177, v177
	v_pk_fma_f32 v[18:19], v[74:75], s[36:37], v[2:3] op_sel_hi:[1,0,1]
	v_med3_f32 v173, v173, s47, v190
	v_min_f32_e32 v19, 0x40e00000, v19
	v_pk_add_f32 v[176:177], v[176:177], 1.0 op_sel_hi:[1,0]
	v_min_f32_e32 v18, 0x40e00000, v18
	v_rcp_f32_e32 v176, v176
	v_rcp_f32_e32 v177, v177
	v_med3_f32 v172, v172, s47, v190
	v_pk_fma_f32 v[172:173], v[172:173], 4.0, 4.0 op_sel_hi:[1,0,0]
	s_mov_b32 s20, 0x24000
	v_pk_mul_f32 v[20:21], v[20:21], v[176:177]
	s_nop 0
	v_pk_mul_f32 v[20:21], v[174:175], v[20:21]
	v_pk_mul_f32 v[174:175], v[18:19], s[78:79] op_sel_hi:[1,0]
	v_cvt_pk_fp8_f32 v23, v20, v21
	v_exp_f32_e32 v174, v174
	v_exp_f32_e32 v175, v175
	v_pk_fma_f32 v[20:21], v[68:69], s[36:37], v[8:9] op_sel_hi:[1,0,1]
	v_pk_fma_f32 v[8:9], v[60:61], s[36:37], v[8:9] op_sel_hi:[1,0,1]
	v_min_f32_e32 v21, 0x40e00000, v21
	v_pk_add_f32 v[174:175], v[174:175], 1.0 op_sel_hi:[1,0]
	v_min_f32_e32 v20, 0x40e00000, v20
	v_rcp_f32_e32 v174, v174
	v_rcp_f32_e32 v175, v175
	v_min_f32_e32 v9, 0x40e00000, v9
	v_min_f32_e32 v8, 0x40e00000, v8
	v_pk_mul_f32 v[18:19], v[18:19], v[174:175]
	v_pk_mul_f32 v[174:175], v[20:21], s[78:79] op_sel_hi:[1,0]
	v_pk_mul_f32 v[18:19], v[172:173], v[18:19]
	v_exp_f32_e32 v174, v174
	v_exp_f32_e32 v175, v175
	v_cvt_pk_fp8_f32 v23, v18, v19 op_sel:[0,0,1]
	v_add_co_u32_e32 v18, vcc, s20, v16
	v_pk_add_f32 v[174:175], v[174:175], 1.0 op_sel_hi:[1,0]
	s_nop 0
	v_addc_co_u32_e32 v19, vcc, 0, v17, vcc
	v_rcp_f32_e32 v174, v174
	v_rcp_f32_e32 v175, v175
	v_pk_fma_f32 v[172:173], v[36:37], s[36:37], v[12:13] op_sel_hi:[1,0,1]
	v_mov_b32_e32 v150, v22
	v_mov_b32_e32 v151, v23
	s_nop 1
	v_permlane16_swap_b32_e32 v148, v150
	v_permlane16_swap_b32_e32 v149, v151
	global_store_dwordx4 v[146:147], v[148:151], off
	v_pk_fma_f32 v[18:19], v[70:71], s[36:37], v[10:11] op_sel_hi:[1,0,1]
	v_med3_f32 v173, v173, s47, v190
	v_med3_f32 v172, v172, s47, v190
	v_pk_mul_f32 v[20:21], v[20:21], v[174:175]
	v_pk_fma_f32 v[172:173], v[172:173], 4.0, 4.0 op_sel_hi:[1,0,0]
	v_min_f32_e32 v19, 0x40e00000, v19
	v_min_f32_e32 v18, 0x40e00000, v18
	v_pk_mul_f32 v[20:21], v[172:173], v[20:21]
	v_pk_mul_f32 v[172:173], v[18:19], s[78:79] op_sel_hi:[1,0]
	v_pk_fma_f32 v[22:23], v[38:39], s[36:37], v[14:15] op_sel_hi:[1,0,1]
	v_exp_f32_e32 v172, v172
	v_exp_f32_e32 v173, v173
	v_med3_f32 v23, v23, s47, v190
	v_med3_f32 v22, v22, s47, v190
	v_pk_fma_f32 v[22:23], v[22:23], 4.0, 4.0 op_sel_hi:[1,0,0]
	v_pk_add_f32 v[172:173], v[172:173], 1.0 op_sel_hi:[1,0]
	v_pk_fma_f32 v[174:175], v[32:33], s[36:37], v[4:5] op_sel_hi:[1,0,1]
	v_rcp_f32_e32 v172, v172
	v_rcp_f32_e32 v173, v173
	v_med3_f32 v175, v175, s47, v190
	v_med3_f32 v174, v174, s47, v190
	v_pk_fma_f32 v[174:175], v[174:175], 4.0, 4.0 op_sel_hi:[1,0,0]
	v_pk_mul_f32 v[18:19], v[18:19], v[172:173]
	v_pk_fma_f32 v[172:173], v[34:35], s[36:37], v[6:7] op_sel_hi:[1,0,1]
	v_pk_mul_f32 v[18:19], v[22:23], v[18:19]
	v_mov_b32_e32 v22, v153
	v_cvt_pk_fp8_f32 v22, v20, v21
; #define LAS __attribute__((address_space(3)))
; template <bool EMU> __device__ __forceinline__ float e2m3q(float y) { if constexpr (EMU) { y = fminf(fmaxf(y, -7.5f), 7.5f); return fabsf(y) < 1.f ? rintf(y * 8.f) * 0.125f : y; } else return y; }
;     static __device__ __forceinline__ f32x2 act2(f32x2 g, f32x2 l) {
;         g = __builtin_elementwise_min(g, (f32x2){7.f, 7.f}); l = __builtin_elementwise_min(__builtin_elementwise_max(l, (f32x2){-7.f, -7.f}), (f32x2){7.f, 7.f});
;         const f32x2 t = g * (-1.702f * 1.44269504089f); f32x2 e; e.x = __builtin_amdgcn_exp2f(t.x); e.y = __builtin_amdgcn_exp2f(t.y);
;         const f32x2 d = e + 1.0f; f32x2 r; r.x = __builtin_amdgcn_rcpf(d.x); r.y = __builtin_amdgcn_rcpf(d.y);
;         return (g * r) * (l * QS_ACT + QS_ACT);
;     __device__ __forceinline__ void operator()(const f32x4 (&acc)[2][2][4][2], const UnitD& u, int wr, int wc, int fr, int fq) const {
;         const int row0 = u.r0 + wr * 64 + fr, col0 = u.c0 + wc * 32 + 8 * fq;
;         const LAS float* bg = bl_lds + u.ui * 256 + wc * 32 + 8 * fq; const LAS float* bl = bg + 128;
;         f32x4 bgv[2], blv[2];
; #pragma unroll
;         for (int n = 0; n < 2; ++n) { bgv[n] = *(const LAS f32x4*)(bg + 4 * n); blv[n] = *(const LAS f32x4*)(bl + 4 * n); }
;         constexpr float SC = 1.f / (QS_X1 * QS_WUP);
; #pragma unroll
;         for (int ai = 0; ai < 2; ++ai)
; #pragma unroll
;             for (int m = 0; m < 4; ++m) { unsigned char* rowp = H + (size_t)(row0 + ai * 128 + m * 16) * DM + col0; u32x2 w;
; #pragma unroll
;                 for (int n = 0; n < 2; ++n) { const f32x4 g = acc[ai][0][m][n] * SC + bgv[n], l = acc[ai][1][m][n] * SC + blv[n];
;                     const f32x2 o0 = act2((f32x2){g[0], g[1]}, (f32x2){l[0], l[1]}), o1 = act2((f32x2){g[2], g[3]}, (f32x2){l[2], l[3]});
;                     int r = 0; r = __builtin_amdgcn_cvt_pk_fp8_f32(e2m3q<EMU_DOWN != 0>(o0.x), e2m3q<EMU_DOWN != 0>(o0.y), r, false); r = __builtin_amdgcn_cvt_pk_fp8_f32(e2m3q<EMU_DOWN != 0>(o1.x), e2m3q<EMU_DOWN != 0>(o1.y), r, true);
;                     if (n == 0) w.x = (unsigned)r; else w.y = (unsigned)r; }
;                 *(u32x2*)rowp = w; }
	v_pk_fma_f32 v[20:21], v[64:65], s[36:37], v[0:1] op_sel_hi:[1,0,1]
	v_mov_b32_e32 v23, v153
	v_min_f32_e32 v21, 0x40e00000, v21
	v_min_f32_e32 v20, 0x40e00000, v20
	v_pk_mul_f32 v[176:177], v[20:21], s[78:79] op_sel_hi:[1,0]
	v_cvt_pk_fp8_f32 v22, v18, v19 op_sel:[0,0,1]
	v_exp_f32_e32 v176, v176
	v_exp_f32_e32 v177, v177
	v_pk_fma_f32 v[18:19], v[66:67], s[36:37], v[2:3] op_sel_hi:[1,0,1]
	v_med3_f32 v173, v173, s47, v190
	v_min_f32_e32 v19, 0x40e00000, v19
	v_pk_add_f32 v[176:177], v[176:177], 1.0 op_sel_hi:[1,0]
	v_min_f32_e32 v18, 0x40e00000, v18
	v_rcp_f32_e32 v176, v176
	v_rcp_f32_e32 v177, v177
	v_med3_f32 v172, v172, s47, v190
	v_pk_fma_f32 v[172:173], v[172:173], 4.0, 4.0 op_sel_hi:[1,0,0]
	s_mov_b32 s20, 0x28000
	v_pk_mul_f32 v[20:21], v[20:21], v[176:177]
	v_pk_fma_f32 v[12:13], v[28:29], s[36:37], v[12:13] op_sel_hi:[1,0,1]
	v_pk_mul_f32 v[20:21], v[174:175], v[20:21]
	v_pk_mul_f32 v[174:175], v[18:19], s[78:79] op_sel_hi:[1,0]
	v_cvt_pk_fp8_f32 v23, v20, v21
	v_exp_f32_e32 v174, v174
	v_exp_f32_e32 v175, v175
	v_pk_fma_f32 v[10:11], v[62:63], s[36:37], v[10:11] op_sel_hi:[1,0,1]
	v_med3_f32 v13, v13, s47, v190
	v_med3_f32 v12, v12, s47, v190
	v_pk_add_f32 v[174:175], v[174:175], 1.0 op_sel_hi:[1,0]
	v_pk_fma_f32 v[14:15], v[30:31], s[36:37], v[14:15] op_sel_hi:[1,0,1]
	v_rcp_f32_e32 v174, v174
	v_rcp_f32_e32 v175, v175
	v_pk_fma_f32 v[12:13], v[12:13], 4.0, 4.0 op_sel_hi:[1,0,0]
	v_min_f32_e32 v11, 0x40e00000, v11
	v_min_f32_e32 v10, 0x40e00000, v10
	v_pk_mul_f32 v[18:19], v[18:19], v[174:175]
	v_pk_fma_f32 v[0:1], v[56:57], s[36:37], v[0:1] op_sel_hi:[1,0,1]
	v_pk_mul_f32 v[18:19], v[172:173], v[18:19]
	v_min_f32_e32 v1, 0x40e00000, v1
	v_cvt_pk_fp8_f32 v23, v18, v19 op_sel:[0,0,1]
	v_add_co_u32_e32 v18, vcc, s20, v16
	v_min_f32_e32 v0, 0x40e00000, v0
	s_nop 0
	v_addc_co_u32_e32 v19, vcc, 0, v17, vcc
	v_mov_b32_e32 v148, v22
	v_mov_b32_e32 v149, v23
	v_lshl_add_u64 v[146:147], v[18:19], 0, v[152:153]
	v_pk_mul_f32 v[18:19], v[8:9], s[78:79] op_sel_hi:[1,0]
	v_pk_fma_f32 v[4:5], v[24:25], s[36:37], v[4:5] op_sel_hi:[1,0,1]
	v_exp_f32_e32 v18, v18
	v_exp_f32_e32 v19, v19
	v_pk_fma_f32 v[2:3], v[58:59], s[36:37], v[2:3] op_sel_hi:[1,0,1]
	v_med3_f32 v5, v5, s47, v190
	v_med3_f32 v4, v4, s47, v190
	v_pk_add_f32 v[18:19], v[18:19], 1.0 op_sel_hi:[1,0]
	v_pk_fma_f32 v[6:7], v[26:27], s[36:37], v[6:7] op_sel_hi:[1,0,1]
	v_rcp_f32_e32 v18, v18
	v_rcp_f32_e32 v19, v19
	v_pk_fma_f32 v[4:5], v[4:5], 4.0, 4.0 op_sel_hi:[1,0,0]
	v_min_f32_e32 v3, 0x40e00000, v3
	v_min_f32_e32 v2, 0x40e00000, v2
	v_pk_mul_f32 v[8:9], v[8:9], v[18:19]
	s_nop 0
	v_pk_mul_f32 v[8:9], v[12:13], v[8:9]
	v_med3_f32 v13, v15, s47, v190
	v_med3_f32 v12, v14, s47, v190
	v_pk_mul_f32 v[14:15], v[10:11], s[78:79] op_sel_hi:[1,0]
	v_pk_fma_f32 v[12:13], v[12:13], 4.0, 4.0 op_sel_hi:[1,0,0]
	v_exp_f32_e32 v14, v14
	v_exp_f32_e32 v15, v15
	s_nop 0
	v_pk_add_f32 v[14:15], v[14:15], 1.0 op_sel_hi:[1,0]
	s_nop 0
	v_rcp_f32_e32 v14, v14
	v_rcp_f32_e32 v15, v15
	s_nop 0
	v_pk_mul_f32 v[10:11], v[10:11], v[14:15]
	s_nop 0
	v_pk_mul_f32 v[10:11], v[12:13], v[10:11]
	v_mov_b32_e32 v12, v153
	v_cvt_pk_fp8_f32 v12, v8, v9
	v_pk_mul_f32 v[8:9], v[0:1], s[78:79] op_sel_hi:[1,0]
	v_mov_b32_e32 v13, v153
	v_exp_f32_e32 v8, v8
	v_exp_f32_e32 v9, v9
	v_cvt_pk_fp8_f32 v12, v10, v11 op_sel:[0,0,1]
	v_pk_add_f32 v[8:9], v[8:9], 1.0 op_sel_hi:[1,0]
	s_nop 0
	v_rcp_f32_e32 v8, v8
	v_rcp_f32_e32 v9, v9
	s_nop 0
	v_pk_mul_f32 v[0:1], v[0:1], v[8:9]
	s_nop 0
	v_pk_mul_f32 v[0:1], v[4:5], v[0:1]
	v_med3_f32 v5, v7, s47, v190
	v_med3_f32 v4, v6, s47, v190
	v_pk_mul_f32 v[6:7], v[2:3], s[78:79] op_sel_hi:[1,0]
	v_cvt_pk_fp8_f32 v13, v0, v1
	v_exp_f32_e32 v6, v6
	v_exp_f32_e32 v7, v7
	v_pk_fma_f32 v[4:5], v[4:5], 4.0, 4.0 op_sel_hi:[1,0,0]
	v_add_co_u32_e32 v0, vcc, 0x2c000, v16
	v_pk_add_f32 v[6:7], v[6:7], 1.0 op_sel_hi:[1,0]
	s_nop 0
	v_addc_co_u32_e32 v1, vcc, 0, v17, vcc
	v_rcp_f32_e32 v6, v6
	v_rcp_f32_e32 v7, v7
	s_andn2_b64 vcc, exec, s[16:17]
	v_pk_mul_f32 v[2:3], v[2:3], v[6:7]
	s_nop 0
	v_pk_mul_f32 v[2:3], v[4:5], v[2:3]
	s_nop 0
	v_cvt_pk_fp8_f32 v13, v2, v3 op_sel:[0,0,1]
	v_mov_b32_e32 v150, v12
	s_nop 0
	v_mov_b32_e32 v151, v13
	s_nop 1
	v_permlane16_swap_b32_e32 v148, v150
	v_permlane16_swap_b32_e32 v149, v151
	global_store_dwordx4 v[146:147], v[148:151], off
	s_cbranch_vccnz .LBB0_759
	s_andn2_b64 vcc, exec, s[4:5]
	s_mov_b32 s86, 0x2f9636c4
	s_cbranch_vccnz .LBB0_758
	s_barrier
